# v44 + pool-claim atomic issued one block early (before the tile loads) in all ten convert loops
# baseline (speedup 1.0000x reference)
.LBB0_24:
	v_cmp_eq_u32_e64 s[0:1], 0, v0
	s_and_saveexec_b64 s[2:3], s[0:1]
	s_cbranch_execz .LBB0_28
	s_mov_b64 s[6:7], exec
	v_mbcnt_lo_u32_b32 v1, s6, 0
	v_mbcnt_hi_u32_b32 v1, s7, v1
	v_cmp_eq_u32_e32 vcc, 0, v1
	s_and_saveexec_b64 s[4:5], vcc
	s_cbranch_execz .LBB0_27
	s_bcnt1_i32_b64 s6, s[6:7]
	v_mov_b32_e32 v3, 0
	v_mov_b32_e32 v4, s6
	global_atomic_add v3, v3, v4, s[94:95] offset:256 sc0
	v_mov_b32_e32 v252, 0
	v_mov_b32_e32 v253, 1
	s_nop 0
	global_atomic_add v253, v252, v253, s[94:95] offset:256 sc0

.LBB0_74:
	s_or_b64 exec, exec, s[28:29]
	s_waitcnt vmcnt(0)
	v_readfirstlane_b32 s10, v253
	s_nop 1
	v_add_u32_e32 v66, s10, v66
	s_branch .LBB0_76

.LBB0_77:
	s_or_b64 exec, exec, s[2:3]
	v_mov_b32_e32 v66, s15
	s_waitcnt lgkmcnt(0)
	s_waitcnt lgkmcnt(0)
	s_barrier
	ds_read_b32 v66, v66
	s_mov_b64 s[68:69], s[18:19]
	s_mov_b32 s25, s21
	s_mov_b32 s27, s23
	s_mov_b32 s26, s22
	s_waitcnt lgkmcnt(0)
	v_cmp_lt_i32_e64 s[2:3], s20, v66
	v_readfirstlane_b32 s60, v66
	s_and_b64 vcc, exec, s[2:3]
	s_mov_b32 s34, s16
	s_mov_b32 s70, s24
	s_mov_b32 s35, s17
	s_cbranch_vccnz .LBB0_101
	s_add_i32 s28, s12, -1
	s_cmp_eq_u32 s28, 0
	s_cbranch_scc1 .Lca0_s
	s_mov_b64 vcc, exec
	s_and_b64 exec, exec, s[0:1]
	v_readlane_b32 s28, v254, 52
	v_readlane_b32 s29, v254, 53
	v_mov_b32_e32 v253, 1
	s_nop 3
	global_atomic_add v253, v73, v253, s[28:29] offset:256 sc0
	s_mov_b64 exec, vcc
.Lca0_s:
	s_cmpk_gt_i32 s60, 0x67f
	s_mov_b64 s[28:29], -1
	s_cbranch_scc0 .LBB0_86
	s_cmpk_gt_u32 s60, 0x7df
	s_cbranch_scc0 .LBB0_83
	s_cmpk_gt_u32 s60, 0x93f
	s_cbranch_scc0 .LBB0_200
	s_add_i32 s59, s60, 0xfffff6c0
	s_mov_b64 s[30:31], s[82:83]
	s_mov_b32 s27, 1
	s_cbranch_execz .LBB0_201

.LBB0_481:
	v_and_b32_e32 v196, 0xf0, v110
	v_add_u32_e32 v197, 0, v52
	v_mul_u32_u24_e32 v198, 0x840, v216
	v_lshl_add_u32 v199, v1, 4, 0
	v_add_u32_e32 v200, 0, v178
	v_mul_u32_u24_e32 v201, 0x210, v193
	v_or_b32_e32 v202, 64, v193
	v_or_b32_e32 v203, 0x60, v193
	v_lshl_add_u32 v204, v216, 4, 0
	v_mul_u32_u24_e32 v235, 0x210, v1
	v_or_b32_e32 v213, 16, v1
	v_or_b32_e32 v209, 32, v1
	v_or_b32_e32 v208, 48, v1
	v_or_b32_e32 v211, 64, v1
	v_or_b32_e32 v210, 0x50, v1
	v_or_b32_e32 v90, 0x60, v1
	s_andn2_b64 vcc, exec, s[2:3]
	v_or_b32_e32 v212, 0x70, v1
	s_cbranch_vccnz .LBB0_705
	s_ashr_i32 s52, s8, 4
	s_cmp_lt_i32 s52, 8
	s_cbranch_scc1 .LBB0_690
	s_and_saveexec_b64 s[2:3], s[0:1]
	v_readlane_b32 s16, v254, 38
	v_readlane_b32 s26, v254, 48
	v_readlane_b32 s27, v254, 49
	v_readlane_b32 s30, v254, 52
	v_readlane_b32 s31, v254, 53
	v_readlane_b32 s17, v254, 39
	v_readlane_b32 s18, v254, 40
	v_readlane_b32 s19, v254, 41
	v_readlane_b32 s20, v254, 42
	v_readlane_b32 s21, v254, 43
	v_readlane_b32 s22, v254, 44
	v_readlane_b32 s23, v254, 45
	v_readlane_b32 s24, v254, 46
	v_readlane_b32 s25, v254, 47
	v_readlane_b32 s28, v254, 50
	v_readlane_b32 s29, v254, 51
	s_cbranch_execz .LBB0_487
	s_mov_b64 s[28:29], exec
	v_mbcnt_lo_u32_b32 v2, s28, 0
	v_mbcnt_hi_u32_b32 v2, s29, v2
	v_cmp_eq_u32_e32 vcc, 0, v2
	s_and_saveexec_b64 s[6:7], vcc
	s_cbranch_execz .LBB0_486
	s_bcnt1_i32_b64 s10, s[28:29]
	v_mov_b32_e32 v3, 0
	v_mov_b32_e32 v4, s10
	global_atomic_add v3, v3, v4, s[30:31] offset:1280 sc0
	v_mov_b32_e32 v252, 0
	v_mov_b32_e32 v253, 1
	s_nop 0
	global_atomic_add v253, v252, v253, s[30:31] offset:1280 sc0

.LBB0_549:
	s_cmp_gt_u32 s16, 20
	v_mov_b32_e32 v66, 0x1690
	s_cbranch_scc1 .LBB0_553
	s_mov_b64 s[30:31], exec
	v_mbcnt_lo_u32_b32 v66, s30, 0
	v_mbcnt_hi_u32_b32 v66, s31, v66
	v_cmp_eq_u32_e32 vcc, 0, v66
	s_and_saveexec_b64 s[28:29], vcc
	s_cbranch_execz .LBB0_552
	s_bcnt1_i32_b64 s11, s[30:31]
	v_readlane_b32 s36, v254, 38
	v_mov_b32_e32 v67, s11
	v_readlane_b32 s50, v254, 52
	v_readlane_b32 s51, v254, 53
	v_readlane_b32 s37, v254, 39
	v_readlane_b32 s38, v254, 40
	v_readlane_b32 s39, v254, 41
	v_readlane_b32 s40, v254, 42
	v_readlane_b32 s41, v254, 43
	v_readlane_b32 s42, v254, 44
	v_readlane_b32 s43, v254, 45
	v_readlane_b32 s44, v254, 46
	v_readlane_b32 s45, v254, 47
	v_readlane_b32 s46, v254, 48
	v_readlane_b32 s47, v254, 49
	v_readlane_b32 s48, v254, 50
	v_readlane_b32 s49, v254, 51
.LBB0_552:
	s_or_b64 exec, exec, s[28:29]
	s_waitcnt vmcnt(0)
	v_readfirstlane_b32 s11, v253
	s_nop 1
	v_add_u32_e32 v66, s11, v66
	v_add_u32_e32 v66, 0x680, v66

.LBB0_554:
	s_or_b64 exec, exec, s[2:3]
	v_mov_b32_e32 v66, s67
	s_waitcnt lgkmcnt(0)
	s_waitcnt lgkmcnt(0)
	s_barrier
	ds_read_b32 v66, v66
	s_movk_i32 s2, 0x168f
	s_mov_b64 s[82:83], s[80:81]
	s_mov_b32 s11, s68
	s_mov_b32 s18, s12
	s_waitcnt lgkmcnt(0)
	v_cmp_lt_i32_e64 s[2:3], s2, v66
	v_readfirstlane_b32 s23, v66
	s_and_b64 vcc, exec, s[2:3]
	s_mov_b32 s13, s69
	s_mov_b32 s21, s78
	s_mov_b32 s84, s10
	s_mov_b32 s20, s19
	s_cbranch_vccnz .LBB0_591
	s_add_i32 s28, s16, 1
	s_cmp_gt_u32 s28, 20
	s_cbranch_scc1 .Lca1_s
	s_mov_b64 vcc, exec
	s_and_b64 exec, exec, s[0:1]
	v_readlane_b32 s28, v254, 52
	v_readlane_b32 s29, v254, 53
	v_mov_b32_e32 v253, 1
	s_nop 3
	global_atomic_add v253, v75, v253, s[28:29] offset:1280 sc0
	s_mov_b64 exec, vcc
.Lca1_s:
	s_cmpk_gt_i32 s23, 0x67f
	s_mov_b64 s[28:29], -1
	s_cbranch_scc0 .LBB0_576
	s_cmpk_gt_u32 s23, 0xa9f
	s_cbranch_scc0 .LBB0_565
	s_add_i32 s11, s23, 0xfffff560
	s_bfe_u32 s13, s11, 0x100007
	s_mulk_i32 s13, 0x2493
	s_lshr_b32 s21, s13, 16
	s_mul_i32 s20, s21, 0xfffffc80
	s_add_i32 s20, s20, s11
	s_cmpk_gt_i32 s20, 0x1bf
	s_mul_hi_u32 s24, s21, 0x3800000
	s_mul_i32 s25, s21, 0x3800000
	s_cbranch_scc0 .LBB0_562
	s_cmpk_gt_u32 s20, 0x37f
	s_cbranch_scc0 .LBB0_560
	v_readlane_b32 s36, v254, 38
	s_add_i32 s22, s20, 0xfffffc80
	v_readlane_b32 s46, v254, 48
	v_readlane_b32 s47, v254, 49
	s_add_u32 s34, s46, s25
	s_addc_u32 s35, s47, s24
	s_mul_i32 s11, s21, 0xe00000
	s_add_u32 s82, s17, s11
	v_readlane_b32 s37, v254, 39
	v_readlane_b32 s38, v254, 40
	v_readlane_b32 s39, v254, 41
	v_readlane_b32 s40, v254, 42
	v_readlane_b32 s41, v254, 43
	v_readlane_b32 s42, v254, 44
	v_readlane_b32 s43, v254, 45
	v_readlane_b32 s44, v254, 46
	v_readlane_b32 s45, v254, 47
	v_readlane_b32 s48, v254, 50
	v_readlane_b32 s49, v254, 51
	v_readlane_b32 s50, v254, 52
	v_readlane_b32 s51, v254, 53
	s_addc_u32 s83, s53, 0
	s_mov_b64 s[28:29], 0

.LBB0_724:
	s_cmpk_lt_i32 s8, 0x80
	s_cselect_b32 s6, 18, 0
	s_and_b64 s[2:3], s[4:5], exec
	s_cselect_b32 s16, s6, 4
	s_cmp_lg_u32 s16, 0
	v_mov_b32_e32 v206, v205
	v_mov_b32_e32 v207, v213
	v_mov_b32_e32 v213, v209
	v_mov_b32_e32 v209, v211
	v_or_b32_e32 v211, 0x60, v1
	s_waitcnt lgkmcnt(0)
	s_barrier
	s_cbranch_scc0 .LBB0_931
	s_and_saveexec_b64 s[2:3], s[0:1]
	v_readlane_b32 s36, v254, 38
	v_readlane_b32 s46, v254, 48
	v_readlane_b32 s47, v254, 49
	v_readlane_b32 s50, v254, 52
	v_readlane_b32 s51, v254, 53
	v_readlane_b32 s37, v254, 39
	v_readlane_b32 s38, v254, 40
	v_readlane_b32 s39, v254, 41
	v_readlane_b32 s40, v254, 42
	v_readlane_b32 s41, v254, 43
	v_readlane_b32 s42, v254, 44
	v_readlane_b32 s43, v254, 45
	v_readlane_b32 s44, v254, 46
	v_readlane_b32 s45, v254, 47
	v_readlane_b32 s48, v254, 50
	v_readlane_b32 s49, v254, 51
	s_cbranch_execz .LBB0_729
	s_mov_b64 s[6:7], exec
	s_waitcnt vmcnt(15)
	v_mbcnt_lo_u32_b32 v2, s6, 0
	v_mbcnt_hi_u32_b32 v2, s7, v2
	v_cmp_eq_u32_e32 vcc, 0, v2
	s_and_saveexec_b64 s[4:5], vcc
	s_cbranch_execz .LBB0_728
	s_bcnt1_i32_b64 s6, s[6:7]
	v_mov_b32_e32 v3, 0
	v_mov_b32_e32 v4, s6
	global_atomic_add v3, v3, v4, s[50:51] offset:1280 sc0
	v_mov_b32_e32 v252, 0
	v_mov_b32_e32 v253, 1
	s_nop 0
	global_atomic_add v253, v252, v253, s[50:51] offset:1280 sc0

.LBB0_795:
	s_or_b64 exec, exec, s[2:3]
	v_mov_b32_e32 v66, s65
	s_waitcnt lgkmcnt(0)
	s_waitcnt lgkmcnt(0)
	s_barrier
	ds_read_b32 v66, v66
	s_movk_i32 s2, 0x168f
	s_mov_b64 s[80:81], s[78:79]
	s_mov_b32 s11, s66
	s_mov_b32 s18, s12
	s_waitcnt lgkmcnt(0)
	v_cmp_lt_i32_e64 s[2:3], s2, v66
	v_readfirstlane_b32 s23, v66
	s_and_b64 vcc, exec, s[2:3]
	s_mov_b32 s13, s67
	s_mov_b32 s21, s74
	s_mov_b32 s82, s10
	s_mov_b32 s20, s19
	s_cbranch_vccnz .LBB0_832
	s_add_i32 s28, s17, 1
	s_cmp_ge_u32 s28, s16
	s_cbranch_scc1 .Lca2_s
	s_mov_b64 vcc, exec
	s_and_b64 exec, exec, s[0:1]
	v_readlane_b32 s28, v254, 52
	v_readlane_b32 s29, v254, 53
	v_mov_b32_e32 v253, 1
	s_nop 3
	global_atomic_add v253, v71, v253, s[28:29] offset:1280 sc0
	s_mov_b64 exec, vcc
.Lca2_s:
	s_cmpk_gt_i32 s23, 0x67f
	s_mov_b64 s[28:29], -1
	s_cbranch_scc0 .LBB0_817
	s_cmpk_gt_u32 s23, 0xa9f
	s_cbranch_scc0 .LBB0_806
	s_add_i32 s11, s23, 0xfffff560
	s_bfe_u32 s13, s11, 0x100007
	s_mulk_i32 s13, 0x2493
	s_lshr_b32 s21, s13, 16
	s_mul_i32 s20, s21, 0xfffffc80
	s_add_i32 s20, s20, s11
	s_cmpk_gt_i32 s20, 0x1bf
	s_mul_hi_u32 s24, s21, 0x3800000
	s_mul_i32 s25, s21, 0x3800000
	s_cbranch_scc0 .LBB0_803
	s_cmpk_gt_u32 s20, 0x37f
	s_cbranch_scc0 .LBB0_801
	v_readlane_b32 s36, v254, 38
	s_add_i32 s22, s20, 0xfffffc80
	v_readlane_b32 s46, v254, 48
	v_readlane_b32 s47, v254, 49
	s_add_u32 s34, s46, s25
	s_addc_u32 s35, s47, s24
	s_mul_i32 s11, s21, 0xe00000
	s_add_u32 s80, s33, s11
	v_readlane_b32 s37, v254, 39
	v_readlane_b32 s38, v254, 40
	v_readlane_b32 s39, v254, 41
	v_readlane_b32 s40, v254, 42
	v_readlane_b32 s41, v254, 43
	v_readlane_b32 s42, v254, 44
	v_readlane_b32 s43, v254, 45
	v_readlane_b32 s44, v254, 46
	v_readlane_b32 s45, v254, 47
	v_readlane_b32 s48, v254, 50
	v_readlane_b32 s49, v254, 51
	v_readlane_b32 s50, v254, 52
	v_readlane_b32 s51, v254, 53
	s_addc_u32 s81, s52, 0
	s_mov_b64 s[28:29], 0

.LBB0_1019:
	s_and_saveexec_b64 s[2:3], s[0:1]
	v_readlane_b32 s16, v254, 38
	v_readlane_b32 s26, v254, 48
	v_readlane_b32 s27, v254, 49
	v_readlane_b32 s30, v254, 52
	v_readlane_b32 s31, v254, 53
	v_readlane_b32 s17, v254, 39
	v_readlane_b32 s18, v254, 40
	v_readlane_b32 s19, v254, 41
	v_readlane_b32 s20, v254, 42
	v_readlane_b32 s21, v254, 43
	v_readlane_b32 s22, v254, 44
	v_readlane_b32 s23, v254, 45
	v_readlane_b32 s24, v254, 46
	v_readlane_b32 s25, v254, 47
	v_readlane_b32 s28, v254, 50
	v_readlane_b32 s29, v254, 51
	s_cbranch_execz .LBB0_1023
	s_mov_b64 s[6:7], exec
	v_mbcnt_lo_u32_b32 v2, s6, 0
	v_mbcnt_hi_u32_b32 v2, s7, v2
	v_cmp_eq_u32_e32 vcc, 0, v2
	s_and_saveexec_b64 s[4:5], vcc
	s_cbranch_execz .LBB0_1022
	s_bcnt1_i32_b64 s6, s[6:7]
	v_mov_b32_e32 v3, 0
	v_mov_b32_e32 v4, s6
	global_atomic_add v3, v3, v4, s[30:31] offset:1280 sc0
	v_mov_b32_e32 v252, 0
	v_mov_b32_e32 v253, 1
	s_nop 0
	global_atomic_add v253, v252, v253, s[30:31] offset:1280 sc0

.LBB0_1087:
	s_or_b64 exec, exec, s[28:29]
	s_waitcnt vmcnt(0)
	v_readfirstlane_b32 s18, v253
	s_nop 1
	v_add_u32_e32 v66, s18, v66
	v_add_u32_e32 v66, 0x680, v66
	s_branch .LBB0_1089

.LBB0_1090:
	s_or_b64 exec, exec, s[2:3]
	v_mov_b32_e32 v66, s64
	s_waitcnt lgkmcnt(0)
	s_waitcnt lgkmcnt(0)
	s_barrier
	ds_read_b32 v66, v66
	s_movk_i32 s2, 0x168f
	s_mov_b64 s[80:81], s[78:79]
	s_mov_b32 s18, s10
	s_mov_b32 s20, s12
	s_waitcnt lgkmcnt(0)
	v_cmp_lt_i32_e64 s[2:3], s2, v66
	v_readfirstlane_b32 s25, v66
	s_and_b64 vcc, exec, s[2:3]
	s_mov_b32 s19, s11
	s_mov_b32 s23, s74
	s_mov_b32 s82, s13
	s_mov_b32 s21, s22
	s_cbranch_vccnz .LBB0_1127
	s_add_i32 s28, s62, -1
	s_cmp_eq_u32 s28, 0
	s_cbranch_scc1 .Lca3_s
	s_mov_b64 vcc, exec
	s_and_b64 exec, exec, s[0:1]
	v_readlane_b32 s28, v254, 52
	v_readlane_b32 s29, v254, 53
	v_mov_b32_e32 v253, 1
	s_nop 3
	global_atomic_add v253, v71, v253, s[28:29] offset:1280 sc0
	s_mov_b64 exec, vcc
.Lca3_s:
	s_cmpk_gt_i32 s25, 0x67f
	s_mov_b64 s[28:29], -1
	s_cbranch_scc0 .LBB0_1112
	s_cmpk_gt_u32 s25, 0xa9f
	s_cbranch_scc0 .LBB0_1101
	s_add_i32 s18, s25, 0xfffff560
	s_bfe_u32 s19, s18, 0x100007
	s_mulk_i32 s19, 0x2493
	s_lshr_b32 s23, s19, 16
	s_mul_i32 s21, s23, 0xfffffc80
	s_add_i32 s21, s21, s18
	s_cmpk_gt_i32 s21, 0x1bf
	s_mul_hi_u32 s26, s23, 0x3800000
	s_mul_i32 s27, s23, 0x3800000
	s_cbranch_scc0 .LBB0_1098
	s_cmpk_gt_u32 s21, 0x37f
	s_cbranch_scc0 .LBB0_1096
	v_readlane_b32 s36, v254, 38
	s_add_i32 s24, s21, 0xfffffc80
	v_readlane_b32 s46, v254, 48
	v_readlane_b32 s47, v254, 49
	s_add_u32 s34, s46, s27
	s_addc_u32 s35, s47, s26
	s_mul_i32 s18, s23, 0xe00000
	s_add_u32 s80, s16, s18
	v_readlane_b32 s37, v254, 39
	v_readlane_b32 s38, v254, 40
	v_readlane_b32 s39, v254, 41
	v_readlane_b32 s40, v254, 42
	v_readlane_b32 s41, v254, 43
	v_readlane_b32 s42, v254, 44
	v_readlane_b32 s43, v254, 45
	v_readlane_b32 s44, v254, 46
	v_readlane_b32 s45, v254, 47
	v_readlane_b32 s48, v254, 50
	v_readlane_b32 s49, v254, 51
	v_readlane_b32 s50, v254, 52
	v_readlane_b32 s51, v254, 53
	s_addc_u32 s81, s17, 0
	s_mov_b64 s[28:29], 0

.LBB0_1507:
	s_cmpk_lg_i32 s9, 0x100
	s_cselect_b64 s[6:7], -1, 0
	s_cmpk_eq_i32 s9, 0x100
	s_cselect_b64 s[0:1], -1, 0
	s_cmpk_lt_i32 s8, 0x80
	s_cselect_b64 s[2:3], -1, 0
	s_and_b64 s[0:1], s[2:3], s[0:1]
	s_and_b64 vcc, exec, s[0:1]
	s_cbranch_vccnz .LBB0_1700
	v_cmp_eq_u32_e64 s[0:1], 0, v0
	s_and_saveexec_b64 s[2:3], s[0:1]
	v_readlane_b32 s36, v254, 38
	v_readlane_b32 s37, v254, 39
	v_readlane_b32 s38, v254, 40
	v_readlane_b32 s39, v254, 41
	v_readlane_b32 s40, v254, 42
	v_readlane_b32 s41, v254, 43
	v_readlane_b32 s42, v254, 44
	v_readlane_b32 s43, v254, 45
	v_readlane_b32 s44, v254, 46
	v_readlane_b32 s45, v254, 47
	v_readlane_b32 s46, v254, 48
	v_readlane_b32 s47, v254, 49
	v_readlane_b32 s48, v254, 50
	v_readlane_b32 s49, v254, 51
	v_readlane_b32 s50, v254, 52
	v_readlane_b32 s51, v254, 53
	s_cbranch_execz .LBB0_1512
	s_mov_b64 s[28:29], exec
	s_waitcnt vmcnt(15)
	v_mbcnt_lo_u32_b32 v2, s28, 0
	v_mbcnt_hi_u32_b32 v2, s29, v2
	v_cmp_eq_u32_e32 vcc, 0, v2
	s_and_saveexec_b64 s[12:13], vcc
	s_cbranch_execz .LBB0_1511
	s_bcnt1_i32_b64 s10, s[28:29]
	v_mov_b32_e32 v3, 0
	v_mov_b32_e32 v4, s10
	global_atomic_add v3, v3, v4, s[50:51] offset:1024 sc0
	v_mov_b32_e32 v252, 0
	v_mov_b32_e32 v253, 1
	s_nop 0
	global_atomic_add v253, v252, v253, s[50:51] offset:1024 sc0

.LBB0_1565:
	s_cmp_ge_u32 s16, s17
	v_mov_b32_e32 v66, 0x680
	s_cbranch_scc1 .LBB0_1569
	s_mov_b64 s[30:31], exec
	v_mbcnt_lo_u32_b32 v66, s30, 0
	v_mbcnt_hi_u32_b32 v66, s31, v66
	v_cmp_eq_u32_e32 vcc, 0, v66
	s_and_saveexec_b64 s[28:29], vcc
	s_cbranch_execz .LBB0_1568
	s_bcnt1_i32_b64 s6, s[30:31]
	v_readlane_b32 s36, v254, 38
	v_mov_b32_e32 v67, s6
	v_readlane_b32 s50, v254, 52
	v_readlane_b32 s51, v254, 53
	v_readlane_b32 s37, v254, 39
	v_readlane_b32 s38, v254, 40
	v_readlane_b32 s39, v254, 41
	v_readlane_b32 s40, v254, 42
	v_readlane_b32 s41, v254, 43
	v_readlane_b32 s42, v254, 44
	v_readlane_b32 s43, v254, 45
	v_readlane_b32 s44, v254, 46
	v_readlane_b32 s45, v254, 47
	v_readlane_b32 s46, v254, 48
	v_readlane_b32 s47, v254, 49
	v_readlane_b32 s48, v254, 50
	v_readlane_b32 s49, v254, 51
.LBB0_1568:
	s_or_b64 exec, exec, s[28:29]
	s_waitcnt vmcnt(0)
	v_readfirstlane_b32 s6, v253
	s_nop 1
	v_add_u32_e32 v66, s6, v66
	v_add_u32_e32 v66, 0x340, v66

.LBB0_1570:
	s_or_b64 exec, exec, s[2:3]
	v_mov_b32_e32 v66, s25
	s_waitcnt lgkmcnt(0)
	s_waitcnt lgkmcnt(0)
	s_barrier
	ds_read_b32 v66, v66
	s_movk_i32 s2, 0x67f
	s_mov_b64 s[86:87], s[84:85]
	s_mov_b32 s53, s26
	s_mov_b32 s55, s33
	s_waitcnt lgkmcnt(0)
	v_cmp_lt_i32_e64 s[2:3], s2, v66
	v_readfirstlane_b32 s31, v66
	s_and_b64 vcc, exec, s[2:3]
	s_mov_b32 s54, s27
	s_mov_b32 s60, s82
	s_mov_b32 s88, s52
	s_mov_b32 s58, s59
	s_cbranch_vccnz .LBB0_1597
	s_add_i32 s28, s16, 1
	s_cmp_ge_u32 s28, s17
	s_cbranch_scc1 .Lca4_s
	s_mov_b64 vcc, exec
	s_and_b64 exec, exec, s[0:1]
	v_readlane_b32 s28, v254, 52
	v_readlane_b32 s29, v254, 53
	v_mov_b32_e32 v253, 1
	s_nop 3
	global_atomic_add v253, v71, v253, s[28:29] offset:1024 sc0
	s_mov_b64 exec, vcc
.Lca4_s:
	s_cmpk_gt_i32 s31, 0x67f
	s_mov_b64 s[28:29], -1
	s_cbranch_scc0 .LBB0_1582
	s_cmpk_gt_u32 s31, 0xa9f
	s_cbranch_scc0 .LBB0_1575
	s_add_i32 s61, s31, 0xfffff560
	s_cmpk_lt_u32 s61, 0x1c0
	s_cbranch_scc1 .LBB0_1580
	v_readlane_b32 s36, v254, 38
	v_readlane_b32 s44, v254, 46
	v_readlane_b32 s45, v254, 47
	s_add_i32 s61, s31, 0xfffff3a0
	s_mov_b32 s54, 1
	v_readlane_b32 s37, v254, 39
	v_readlane_b32 s38, v254, 40
	v_readlane_b32 s39, v254, 41
	v_readlane_b32 s40, v254, 42
	v_readlane_b32 s41, v254, 43
	v_readlane_b32 s42, v254, 44
	v_readlane_b32 s43, v254, 45
	v_readlane_b32 s46, v254, 48
	v_readlane_b32 s47, v254, 49
	v_readlane_b32 s48, v254, 50
	v_readlane_b32 s49, v254, 51
	v_readlane_b32 s50, v254, 52
	v_readlane_b32 s51, v254, 53
	s_mov_b64 s[34:35], s[44:45]
	s_mov_b64 s[28:29], 0

.LBB0_2049:
	v_and_b32_e32 v196, 0xf0, v103
	v_add_u32_e32 v197, 0, v46
	v_mul_u32_u24_e32 v198, 0x840, v216
	v_lshl_add_u32 v199, v1, 4, 0
	v_add_u32_e32 v200, 0, v178
	v_mul_u32_u24_e32 v201, 0x210, v193
	v_or_b32_e32 v202, 64, v193
	v_or_b32_e32 v203, 0x60, v193
	v_lshl_add_u32 v204, v216, 4, 0
	v_mul_u32_u24_e32 v235, 0x210, v1
	v_or_b32_e32 v213, 16, v1
	v_or_b32_e32 v209, 32, v1
	v_or_b32_e32 v208, 48, v1
	v_or_b32_e32 v211, 64, v1
	v_or_b32_e32 v210, 0x50, v1
	v_or_b32_e32 v97, 0x60, v1
	s_andn2_b64 vcc, exec, s[2:3]
	v_or_b32_e32 v212, 0x70, v1
	s_cbranch_vccnz .LBB0_2273
	s_ashr_i32 s16, s8, 4
	s_cmp_lt_i32 s16, 8
	s_cbranch_scc1 .LBB0_2258
	s_and_saveexec_b64 s[2:3], s[0:1]
	v_readlane_b32 s36, v254, 38
	v_readlane_b32 s37, v254, 39
	v_readlane_b32 s38, v254, 40
	v_readlane_b32 s39, v254, 41
	v_readlane_b32 s42, v254, 44
	v_readlane_b32 s43, v254, 45
	v_readlane_b32 s44, v254, 46
	v_readlane_b32 s45, v254, 47
	v_readlane_b32 s46, v254, 48
	v_readlane_b32 s47, v254, 49
	v_readlane_b32 s50, v254, 52
	v_readlane_b32 s51, v254, 53
	v_readlane_b32 s40, v254, 42
	v_readlane_b32 s41, v254, 43
	v_readlane_b32 s48, v254, 50
	v_readlane_b32 s49, v254, 51
	s_cbranch_execz .LBB0_2055
	s_mov_b64 s[20:21], exec
	v_mbcnt_lo_u32_b32 v2, s20, 0
	v_mbcnt_hi_u32_b32 v2, s21, v2
	v_cmp_eq_u32_e32 vcc, 0, v2
	s_and_saveexec_b64 s[6:7], vcc
	s_cbranch_execz .LBB0_2054
	s_bcnt1_i32_b64 s10, s[20:21]
	v_mov_b32_e32 v3, 0
	v_mov_b32_e32 v4, s10
	global_atomic_add v3, v3, v4, s[50:51] offset:1536 sc0
	v_mov_b32_e32 v252, 0
	v_mov_b32_e32 v253, 1
	s_nop 0
	global_atomic_add v253, v252, v253, s[50:51] offset:1536 sc0

.LBB0_2117:
	s_cmp_gt_u32 s17, 20
	v_mov_b32_e32 v66, 0x26a0
	s_cbranch_scc1 .LBB0_2121
	s_mov_b64 s[30:31], exec
	v_mbcnt_lo_u32_b32 v66, s30, 0
	v_mbcnt_hi_u32_b32 v66, s31, v66
	v_cmp_eq_u32_e32 vcc, 0, v66
	s_and_saveexec_b64 s[28:29], vcc
	s_cbranch_execz .LBB0_2120
	s_bcnt1_i32_b64 s22, s[30:31]
	v_readlane_b32 s36, v254, 38
	v_mov_b32_e32 v67, s22
	v_readlane_b32 s50, v254, 52
	v_readlane_b32 s51, v254, 53
	v_readlane_b32 s37, v254, 39
	v_readlane_b32 s38, v254, 40
	v_readlane_b32 s39, v254, 41
	v_readlane_b32 s40, v254, 42
	v_readlane_b32 s41, v254, 43
	v_readlane_b32 s42, v254, 44
	v_readlane_b32 s43, v254, 45
	v_readlane_b32 s44, v254, 46
	v_readlane_b32 s45, v254, 47
	v_readlane_b32 s46, v254, 48
	v_readlane_b32 s47, v254, 49
	v_readlane_b32 s48, v254, 50
	v_readlane_b32 s49, v254, 51
.LBB0_2120:
	s_or_b64 exec, exec, s[28:29]
	s_waitcnt vmcnt(0)
	v_readfirstlane_b32 s22, v253
	s_nop 1
	v_add_u32_e32 v66, s22, v66
	v_add_u32_e32 v66, 0x1690, v66

.LBB0_2122:
	s_or_b64 exec, exec, s[2:3]
	v_mov_b32_e32 v66, s82
	s_waitcnt lgkmcnt(0)
	s_waitcnt lgkmcnt(0)
	s_barrier
	ds_read_b32 v66, v66
	s_movk_i32 s2, 0x269f
	s_mov_b64 s[78:79], s[76:77]
	s_mov_b32 s22, s10
	s_mov_b32 s24, s18
	s_waitcnt lgkmcnt(0)
	v_cmp_lt_i32_e64 s[2:3], s2, v66
	v_readfirstlane_b32 s31, v66
	s_and_b64 vcc, exec, s[2:3]
	s_mov_b32 s23, s11
	s_mov_b32 s83, s68
	s_mov_b32 s80, s19
	s_mov_b32 s25, s69
	s_cbranch_vccnz .LBB0_2159
	s_add_i32 s28, s17, 1
	s_cmp_gt_u32 s28, 20
	s_cbranch_scc1 .Lca5_s
	s_mov_b64 vcc, exec
	s_and_b64 exec, exec, s[0:1]
	v_readlane_b32 s28, v254, 52
	v_readlane_b32 s29, v254, 53
	v_mov_b32_e32 v253, 1
	s_nop 3
	global_atomic_add v253, v75, v253, s[28:29] offset:1536 sc0
	s_mov_b64 exec, vcc
.Lca5_s:
	s_cmpk_gt_i32 s31, 0x67f
	s_mov_b64 s[28:29], -1
	s_cbranch_scc0 .LBB0_2144
	s_cmpk_gt_u32 s31, 0xa9f
	s_cbranch_scc0 .LBB0_2133
	s_add_i32 s22, s31, 0xfffff560
	s_bfe_u32 s23, s22, 0x100007
	s_mulk_i32 s23, 0x2493
	s_lshr_b32 s30, s23, 16
	s_mul_i32 s25, s30, 0xfffffc80
	s_add_i32 s25, s25, s22
	s_cmpk_gt_i32 s25, 0x1bf
	s_mul_hi_u32 s81, s30, 0x3800000
	s_mul_i32 s83, s30, 0x3800000
	s_cbranch_scc0 .LBB0_2130
	s_cmpk_gt_u32 s25, 0x37f
	s_cbranch_scc0 .LBB0_2128
	v_readlane_b32 s36, v254, 38
	s_add_i32 s80, s25, 0xfffffc80
	v_readlane_b32 s46, v254, 48
	v_readlane_b32 s47, v254, 49
	s_add_u32 s34, s46, s83
	s_addc_u32 s35, s47, s81
	s_mul_i32 s22, s30, 0xe00000
	s_add_u32 s78, s27, s22
	v_readlane_b32 s37, v254, 39
	v_readlane_b32 s38, v254, 40
	v_readlane_b32 s39, v254, 41
	v_readlane_b32 s40, v254, 42
	v_readlane_b32 s41, v254, 43
	v_readlane_b32 s42, v254, 44
	v_readlane_b32 s43, v254, 45
	v_readlane_b32 s44, v254, 46
	v_readlane_b32 s45, v254, 47
	v_readlane_b32 s48, v254, 50
	v_readlane_b32 s49, v254, 51
	v_readlane_b32 s50, v254, 52
	v_readlane_b32 s51, v254, 53
	s_addc_u32 s79, s54, 0
	s_mov_b64 s[28:29], 0

.LBB0_2292:
	s_cmpk_lt_i32 s8, 0x80
	s_cselect_b32 s6, 18, 0
	s_and_b64 s[2:3], s[4:5], exec
	s_cselect_b32 s33, s6, 4
	s_cmp_lg_u32 s33, 0
	v_mov_b32_e32 v206, v205
	v_mov_b32_e32 v207, v213
	v_mov_b32_e32 v213, v209
	v_mov_b32_e32 v209, v211
	v_or_b32_e32 v211, 0x60, v1
	s_waitcnt lgkmcnt(0)
	s_barrier
	s_cbranch_scc0 .LBB0_2499
	s_and_saveexec_b64 s[2:3], s[0:1]
	s_cbranch_execz .LBB0_2297
	s_mov_b64 s[6:7], exec
	s_waitcnt vmcnt(15)
	v_mbcnt_lo_u32_b32 v2, s6, 0
	v_mbcnt_hi_u32_b32 v2, s7, v2
	v_cmp_eq_u32_e32 vcc, 0, v2
	s_and_saveexec_b64 s[4:5], vcc
	s_cbranch_execz .LBB0_2296
	s_bcnt1_i32_b64 s6, s[6:7]
	v_mov_b32_e32 v3, 0
	v_mov_b32_e32 v4, s6
	global_atomic_add v3, v3, v4, s[94:95] offset:1536 sc0
	v_mov_b32_e32 v252, 0
	v_mov_b32_e32 v253, 1
	s_nop 0
	global_atomic_add v253, v252, v253, s[94:95] offset:1536 sc0

.LBB0_2361:
	s_or_b64 exec, exec, s[28:29]
	s_waitcnt vmcnt(0)
	v_readfirstlane_b32 s18, v253
	s_nop 1
	v_add_u32_e32 v66, s18, v66
	v_add_u32_e32 v66, 0x1690, v66

.LBB0_2363:
	s_or_b64 exec, exec, s[2:3]
	v_mov_b32_e32 v66, s71
	s_waitcnt lgkmcnt(0)
	s_waitcnt lgkmcnt(0)
	s_barrier
	ds_read_b32 v66, v66
	s_movk_i32 s2, 0x269f
	s_mov_b64 s[52:53], s[26:27]
	s_mov_b32 s24, s10
	s_mov_b32 s76, s22
	s_waitcnt lgkmcnt(0)
	v_cmp_lt_i32_e64 s[2:3], s2, v66
	v_readfirstlane_b32 s31, v66
	s_and_b64 vcc, exec, s[2:3]
	s_mov_b32 s25, s11
	s_mov_b32 s78, s20
	s_mov_b32 s54, s23
	s_mov_b32 s77, s21
	s_cbranch_vccnz .LBB0_2400
	s_add_i32 s28, s17, 1
	s_cmp_ge_u32 s28, s33
	s_cbranch_scc1 .Lca6_s
	s_mov_b64 vcc, exec
	s_and_b64 exec, exec, s[0:1]
	v_readlane_b32 s28, v254, 52
	v_readlane_b32 s29, v254, 53
	v_mov_b32_e32 v253, 1
	s_nop 3
	global_atomic_add v253, v71, v253, s[28:29] offset:1536 sc0
	s_mov_b64 exec, vcc
.Lca6_s:
	s_cmpk_gt_i32 s31, 0x67f
	s_mov_b64 s[28:29], -1
	s_cbranch_scc0 .LBB0_2385
	s_cmpk_gt_u32 s31, 0xa9f
	s_cbranch_scc0 .LBB0_2374
	s_add_i32 s18, s31, 0xfffff560
	s_bfe_u32 s24, s18, 0x100007
	s_mulk_i32 s24, 0x2493
	s_lshr_b32 s55, s24, 16
	s_mul_i32 s30, s55, 0xfffffc80
	s_add_i32 s30, s30, s18
	s_cmpk_gt_i32 s30, 0x1bf
	s_mul_hi_u32 s77, s55, 0x3800000
	s_mul_i32 s78, s55, 0x3800000
	s_cbranch_scc0 .LBB0_2371
	s_cmpk_gt_u32 s30, 0x37f
	s_cbranch_scc0 .LBB0_2369
	s_add_i32 s54, s30, 0xfffffc80
	s_add_u32 s34, s90, s78
	s_addc_u32 s35, s91, s77
	s_mul_i32 s18, s55, 0xe00000
	s_add_u32 s52, s58, s18
	s_addc_u32 s53, s59, 0
	s_mov_b64 s[28:29], 0

.LBB0_2588:
	s_mov_b64 s[6:7], exec
	v_mbcnt_lo_u32_b32 v2, s6, 0
	v_mbcnt_hi_u32_b32 v2, s7, v2
	v_cmp_eq_u32_e32 vcc, 0, v2
	s_and_saveexec_b64 s[4:5], vcc
	s_cbranch_execz .LBB0_2590
	s_bcnt1_i32_b64 s6, s[6:7]
	v_mov_b32_e32 v3, 0
	v_mov_b32_e32 v4, s6
	global_atomic_add v3, v3, v4, s[94:95] offset:1536 sc0
	v_mov_b32_e32 v252, 0
	v_mov_b32_e32 v253, 1
	s_nop 0
	global_atomic_add v253, v252, v253, s[94:95] offset:1536 sc0

.LBB0_2655:
	s_or_b64 exec, exec, s[28:29]
	s_waitcnt vmcnt(0)
	v_readfirstlane_b32 s18, v253
	s_nop 1
	v_add_u32_e32 v66, s18, v66
	v_add_u32_e32 v66, 0x1690, v66
	s_branch .LBB0_2657

.LBB0_2658:
	s_or_b64 exec, exec, s[2:3]
	v_mov_b32_e32 v66, s70
	s_waitcnt lgkmcnt(0)
	s_waitcnt lgkmcnt(0)
	s_barrier
	ds_read_b32 v66, v66
	s_movk_i32 s2, 0x269f
	s_mov_b64 s[52:53], s[26:27]
	s_mov_b32 s24, s10
	s_mov_b32 s71, s22
	s_waitcnt lgkmcnt(0)
	v_cmp_lt_i32_e64 s[2:3], s2, v66
	v_readfirstlane_b32 s31, v66
	s_and_b64 vcc, exec, s[2:3]
	s_mov_b32 s25, s11
	s_mov_b32 s77, s20
	s_mov_b32 s54, s23
	s_mov_b32 s76, s21
	s_cbranch_vccnz .LBB0_2695
	s_add_i32 s28, s68, -1
	s_cmp_eq_u32 s28, 0
	s_cbranch_scc1 .Lca7_s
	s_mov_b64 vcc, exec
	s_and_b64 exec, exec, s[0:1]
	v_readlane_b32 s28, v254, 52
	v_readlane_b32 s29, v254, 53
	v_mov_b32_e32 v253, 1
	s_nop 3
	global_atomic_add v253, v71, v253, s[28:29] offset:1536 sc0
	s_mov_b64 exec, vcc
.Lca7_s:
	s_cmpk_gt_i32 s31, 0x67f
	s_mov_b64 s[28:29], -1
	s_cbranch_scc0 .LBB0_2680
	s_cmpk_gt_u32 s31, 0xa9f
	s_cbranch_scc0 .LBB0_2669
	s_add_i32 s18, s31, 0xfffff560
	s_bfe_u32 s24, s18, 0x100007
	s_mulk_i32 s24, 0x2493
	s_lshr_b32 s55, s24, 16
	s_mul_i32 s30, s55, 0xfffffc80
	s_add_i32 s30, s30, s18
	s_cmpk_gt_i32 s30, 0x1bf
	s_mul_hi_u32 s76, s55, 0x3800000
	s_mul_i32 s77, s55, 0x3800000
	s_cbranch_scc0 .LBB0_2666
	s_cmpk_gt_u32 s30, 0x37f
	s_cbranch_scc0 .LBB0_2664
	s_add_i32 s54, s30, 0xfffffc80
	s_add_u32 s34, s90, s77
	s_addc_u32 s35, s91, s76
	s_mul_i32 s18, s55, 0xe00000
	s_add_u32 s52, s17, s18
	s_addc_u32 s53, s33, 0
	s_mov_b64 s[28:29], 0

.LBB0_3126:
	s_or_b64 exec, exec, s[2:3]
	s_cmpk_lg_i32 s9, 0x100
	s_cselect_b32 s33, s9, 0xf0
	s_waitcnt lgkmcnt(0)
	s_cmp_lt_i32 s8, s33
	s_cselect_b64 s[4:5], -1, 0
	s_and_b64 vcc, exec, s[4:5]
	s_waitcnt lgkmcnt(0)
	s_barrier
	s_cbranch_vccnz .LBB0_3342
	s_and_saveexec_b64 s[2:3], s[0:1]
	s_cbranch_execz .LBB0_3131
	s_mov_b64 s[10:11], exec
	v_mbcnt_lo_u32_b32 v1, s10, 0
	v_mbcnt_hi_u32_b32 v1, s11, v1
	v_cmp_eq_u32_e32 vcc, 0, v1
	s_and_saveexec_b64 s[6:7], vcc
	s_cbranch_execz .LBB0_3130
	s_bcnt1_i32_b64 s10, s[10:11]
	s_waitcnt vmcnt(15)
	v_mov_b32_e32 v2, 0
	v_mov_b32_e32 v3, s10
	global_atomic_add v2, v2, v3, s[94:95] offset:2048 sc0
	v_mov_b32_e32 v252, 0
	v_mov_b32_e32 v253, 1
	s_nop 0
	global_atomic_add v253, v252, v253, s[94:95] offset:2048 sc0

.LBB0_3199:
	s_or_b64 exec, exec, s[20:21]
	s_waitcnt vmcnt(0)
	v_readfirstlane_b32 s6, v253
	s_nop 1
	v_add_u32_e32 v66, s6, v66
	v_add_u32_e32 v66, 0x26a0, v66
	s_branch .LBB0_3201

.LBB0_3202:
	s_or_b64 exec, exec, s[2:3]
	v_mov_b32_e32 v66, s61
	s_waitcnt lgkmcnt(0)
	s_waitcnt lgkmcnt(0)
	s_barrier
	ds_read_b32 v66, v66
	s_mov_b64 s[20:21], s[18:19]
	s_mov_b32 s65, s24
	s_mov_b32 s67, s63
	s_mov_b32 s66, s25
	s_waitcnt lgkmcnt(0)
	v_cmp_lt_i32_e64 s[2:3], s62, v66
	v_readfirstlane_b32 s28, v66
	s_and_b64 vcc, exec, s[2:3]
	s_mov_b32 s69, s16
	s_mov_b32 s22, s64
	s_mov_b32 s68, s17
	s_cbranch_vccnz .LBB0_3243
	s_add_i32 s22, s59, -1
	s_cmp_eq_u32 s22, 0
	s_cbranch_scc1 .Lca8_s
	s_mov_b64 vcc, exec
	s_and_b64 exec, exec, s[0:1]
	v_readlane_b32 s22, v254, 52
	v_readlane_b32 s23, v254, 53
	v_mov_b32_e32 v253, 1
	s_nop 3
	global_atomic_add v253, v71, v253, s[22:23] offset:2048 sc0
	s_mov_b64 exec, vcc
.Lca8_s:
	s_cmpk_gt_i32 s28, 0x67f
	s_mov_b64 s[22:23], -1
	s_cbranch_scc0 .LBB0_3228
	s_cmpk_gt_u32 s28, 0xa9f
	s_cbranch_scc0 .LBB0_3217
	s_cmpk_gt_u32 s28, 0x269f
	s_mov_b64 s[20:21], -1
	s_cbranch_scc0 .LBB0_3207
	s_add_i32 s6, s28, 0xd960
	s_bfe_u32 s6, s6, 0xa0006
	s_mulk_i32 s6, 0x2493
	s_lshr_b32 s68, s6, 16
	s_mul_i32 s6, s68, 0xfffffe40
	s_add_i32 s6, s28, s6
	s_add_i32 s29, s6, 0xffffdce0
	s_cbranch_execnz .LBB0_3209
	s_branch .LBB0_3208

.LBB0_3369:
	s_and_saveexec_b64 s[2:3], s[0:1]
	s_cbranch_execz .LBB0_3373
	s_mov_b64 s[6:7], exec
	v_mbcnt_lo_u32_b32 v1, s6, 0
	v_mbcnt_hi_u32_b32 v1, s7, v1
	v_cmp_eq_u32_e32 vcc, 0, v1
	s_and_saveexec_b64 s[4:5], vcc
	s_cbranch_execz .LBB0_3372
	s_bcnt1_i32_b64 s6, s[6:7]
	s_waitcnt vmcnt(15)
	v_mov_b32_e32 v2, 0
	v_mov_b32_e32 v3, s6
	global_atomic_add v2, v2, v3, s[94:95] offset:2048 sc0
	v_mov_b32_e32 v252, 0
	v_mov_b32_e32 v253, 1
	s_nop 0
	global_atomic_add v253, v252, v253, s[94:95] offset:2048 sc0

.LBB0_3441:
	s_or_b64 exec, exec, s[18:19]
	s_waitcnt vmcnt(0)
	v_readfirstlane_b32 s4, v253
	s_nop 1
	v_add_u32_e32 v66, s4, v66
	v_add_u32_e32 v66, 0x26a0, v66
	s_branch .LBB0_3443

.LBB0_3444:
	s_or_b64 exec, exec, s[2:3]
	v_mov_b32_e32 v66, s58
	s_waitcnt lgkmcnt(0)
	s_waitcnt lgkmcnt(0)
	s_barrier
	ds_read_b32 v66, v66
	s_mov_b64 s[18:19], s[16:17]
	s_mov_b32 s62, s24
	s_mov_b32 s64, s60
	s_mov_b32 s63, s25
	s_waitcnt lgkmcnt(0)
	v_cmp_lt_i32_e64 s[2:3], s59, v66
	v_readfirstlane_b32 s26, v66
	s_and_b64 vcc, exec, s[2:3]
	s_mov_b32 s66, s14
	s_mov_b32 s20, s61
	s_mov_b32 s65, s15
	s_cbranch_vccnz .LBB0_3485
	s_add_i32 s20, s54, -1
	s_cmp_eq_u32 s20, 0
	s_cbranch_scc1 .Lca9_s
	s_mov_b64 vcc, exec
	s_and_b64 exec, exec, s[0:1]
	v_readlane_b32 s20, v254, 52
	v_readlane_b32 s21, v254, 53
	v_mov_b32_e32 v253, 1
	s_nop 3
	global_atomic_add v253, v71, v253, s[20:21] offset:2048 sc0
	s_mov_b64 exec, vcc
.Lca9_s:
	s_cmpk_gt_i32 s26, 0x67f
	s_mov_b64 s[20:21], -1
	s_cbranch_scc0 .LBB0_3470
	s_cmpk_gt_u32 s26, 0xa9f
	s_cbranch_scc0 .LBB0_3459
	s_cmpk_gt_u32 s26, 0x269f
	s_mov_b64 s[18:19], -1
	s_cbranch_scc0 .LBB0_3449
	s_add_i32 s4, s26, 0xd960
	s_bfe_u32 s4, s4, 0xa0006
	s_mulk_i32 s4, 0x2493
	s_lshr_b32 s65, s4, 16
	s_mul_i32 s4, s65, 0xfffffe40
	s_add_i32 s4, s26, s4
	s_add_i32 s27, s4, 0xffffdce0
	s_cbranch_execnz .LBB0_3451
	s_branch .LBB0_3450
